# Y0 rows 0-95 deferred to scan 3 (producer waves), y-writer scan-1 stores masked, single-round 32-row epilogue gather, extra vmcnt(0) guard in y-writer
# baseline (speedup 1.0000x reference)
.LBB1_104:
	s_mov_b32 s3, 6
	s_mov_b64 s[8:9], 0
	s_mov_b32 s5, 0
	s_barrier
	s_waitcnt vmcnt(0)
	s_branch .LBB1_106
